# gather: LN1/LN2 gain+bias vectors staged in LDS once per phase; 32 per-token L2 loads become ds_read_b128 (removes serialized vmcnt(0) round trips)
# speedup vs baseline: 1.0508x; 1.0355x over previous
; __device__ __forceinline__ int fresh_lane() { unsigned z = 0u; asm volatile("" : "+v"(z)); return (int)__builtin_amdgcn_mbcnt_hi(~0u, __builtin_amdgcn_mbcnt_lo(~0u, z)); }
; #define GATHER_ISSUE(k, sn_) do { const int sn = (sn_); const int secn = (sn >> 6) & 3; \
;         const int idsel = (sn >= 256) ? id0n : ((secn & 1) ? id1 : id0); \
;         const unsigned so = (unsigned)__builtin_amdgcn_readlane(idsel, sn & 63) * ROW4 + ((secn >= 2) ? TAB4 : 0u); \
;         ring[k] = __builtin_bit_cast(v4u, __builtin_amdgcn_raw_buffer_load_b128(rs, voff, so, 0)); } while (0)
;     const unsigned char* UV4 = (const unsigned char*)(F.ws + WS_UB) + (size_t)layer * (2u * TAB4);
;     const bf16* ZB = (const bf16*)(F.ws + WS_ZF); const bf16* PLE = (const bf16*)(F.ws + WS_PLE);
;     const int* IDX = (const int*)(F.ws + WS_IDX); const float* GWt = (const float*)(F.ws + WS_GW);
;     float* OF = (layer == 3 && !dummy) ? F.out : (float*)nullptr; bf16* XB = (bf16*)(F.ws + (dummy ? WS_X1B : WS_XB));
;     ...
;     const int idmask = (dummy == 1) ? PROBE_GATHER_MASK : 0x3fff;
;     ...
;     const float* gain1 = F.ln_gain + (size_t)(layer * 2) * D; const float* bias1 = F.ln_bias + (size_t)(layer * 2) * D;
;     const float* gain = F.ln_gain + (size_t)(layer * 2 + 1) * D; const float* bias = F.ln_bias + (size_t)(layer * 2 + 1) * D;
;     const int lane = fresh_lane();
;     const bool b3 = (lane & 8) != 0, b2 = (lane & 4) != 0, b1 = (lane & 2) != 0, b0 = (lane & 1) != 0;
;     const __amdgpu_buffer_rsrc_t rs = __builtin_amdgcn_make_buffer_rsrc((void*)UV4, (short)0, (int)(2u * TAB4), 0x00020000);
;     const unsigned voff = (unsigned)lane * 16u;
;     v4u ring[16];
;     int id0 = 0, id1 = 0, id0n = 0;
;     ...
;     int id1n = 0; float g0n = 0.f, g1n = 0.f;
;     if (F.gw < T) { gather_sorted_ids(IDX, GWt, F.gw, lane, id0n, id1n, g0n, g1n);
;     ...
;         id0n &= idmask; id1n &= idmask;
;     ...
; #pragma unroll
;         for (int k = 0; k < 16; ++k) GATHER_ISSUE(k, 256 + k); }
.LBB0_1412:
	s_andn2_b64 vcc, exec, s[14:15]
	s_cbranch_vccnz .LBB0_1452
	s_add_u32 s8, s60, 0x4a600000
	v_writelane_b32 v254, s8, 56
	s_addc_u32 s8, s61, 0
	v_writelane_b32 v255, s8, 5
	s_add_u32 s8, s60, 0x66600000
	v_writelane_b32 v255, s8, 7
	s_addc_u32 s8, s61, 0
	s_cmp_eq_u32 s18, 3
	v_writelane_b32 v255, s8, 9
	s_cselect_b64 s[8:9], -1, 0
	s_add_u32 s10, s60, 0x36600000
	v_writelane_b32 v255, s10, 11
	s_addc_u32 s43, s61, 0
	s_lshl_b32 s10, s18, 1
	s_mov_b64 s[16:17], s[80:81]
	v_writelane_b32 v255, s76, 1
	s_mov_b64 s[18:19], s[82:83]
	s_mov_b64 s[20:21], s[84:85]
	s_mov_b64 s[22:23], s[86:87]
	v_writelane_b32 v255, s77, 2
	v_readlane_b32 s76, v254, 1
	s_ashr_i32 s11, s10, 31
	v_readlane_b32 s90, v254, 15
	v_readlane_b32 s91, v254, 16
	s_lshl_b64 s[12:13], s[10:11], 13
	s_mov_b64 s[14:15], s[90:91]
	s_add_u32 s36, s14, s12
	s_addc_u32 s37, s15, s13
	s_add_u32 s12, s16, s12
	s_addc_u32 s13, s17, s13
	s_or_b32 s10, s10, 1
	v_readlane_b32 s72, v255, 1
	s_ashr_i32 s11, s10, 31
	v_readlane_b32 s73, v255, 2
	v_writelane_b32 v255, s12, 13
	s_lshl_b64 s[10:11], s[10:11], 13
	v_readlane_b32 s80, v254, 5
	v_writelane_b32 v255, s13, 14
	s_add_u32 s12, s14, s10
	s_addc_u32 s13, s15, s11
	v_readlane_b32 s81, v254, 6
	s_add_u32 s80, s16, s10
	s_addc_u32 s81, s17, s11
	v_readlane_b32 s10, v254, 51
	v_readlane_b32 s82, v254, 7
	v_readlane_b32 s83, v254, 8
	v_readlane_b32 s11, v254, 52
	s_and_b64 s[82:83], s[8:9], s[10:11]
	s_add_u32 s30, s60, 0x57600000
	v_writelane_b32 v255, s12, 15
	s_addc_u32 s39, s61, 0
	s_add_u32 s8, s60, 0x53200000
	v_writelane_b32 v255, s13, 16
	v_writelane_b32 v255, s8, 33
	s_addc_u32 s8, s61, 0
	v_writelane_b32 v255, s8, 35
	s_add_u32 s8, s60, 0x53600000
	v_writelane_b32 v255, s8, 29
	s_addc_u32 s8, s61, 0
	v_cmp_eq_u32_e64 s[28:29], 0, v68
	v_cmp_eq_u32_e32 vcc, 0, v67
	v_writelane_b32 v255, s8, 31
	s_xor_b64 s[44:45], vcc, s[28:29]
	v_cmp_eq_u32_e64 s[20:21], 0, v69
	v_writelane_b32 v255, s44, 17
	v_lshlrev_b32_e32 v70, 5, v130
	v_ashrrev_i32_e32 v71, 31, v70
	v_writelane_b32 v255, s45, 18
	s_xor_b64 s[44:45], vcc, s[20:21]
	v_writelane_b32 v255, s44, 19
	v_add_u32_e32 v194, 4, v66
	v_add_u32_e32 v195, 8, v66
	v_writelane_b32 v255, s45, 20
	s_xor_b64 s[44:45], vcc, s[0:1]
	v_writelane_b32 v255, s44, 21
	v_add_u32_e32 v196, 12, v66
	v_lshl_add_u64 v[66:67], s[60:61], 0, v[70:71]
	v_writelane_b32 v255, s45, 22
	s_xor_b64 s[44:45], vcc, s[2:3]
	v_writelane_b32 v255, s44, 23
	s_xor_b64 s[8:9], s[4:5], s[6:7]
	s_xor_b64 s[10:11], s[2:3], s[4:5]
	v_writelane_b32 v255, s45, 24
	s_xor_b64 s[44:45], vcc, s[4:5]
	v_writelane_b32 v255, s44, 25
	s_xor_b64 s[12:13], s[2:3], s[6:7]
	s_xor_b64 s[14:15], s[0:1], s[2:3]
	v_writelane_b32 v255, s45, 26
	s_xor_b64 s[44:45], vcc, s[6:7]
	v_writelane_b32 v255, s44, 27
	s_xor_b64 s[16:17], s[0:1], s[4:5]
	s_xor_b64 s[18:19], s[0:1], s[6:7]
	v_writelane_b32 v255, s45, 28
	s_mov_b64 s[44:45], 0x55600000
	s_xor_b64 s[22:23], s[20:21], s[0:1]
	s_xor_b64 s[24:25], s[20:21], s[2:3]
	s_xor_b64 s[26:27], s[20:21], s[4:5]
	v_ashrrev_i32_e32 v193, 4, v130
	v_lshl_add_u64 v[132:133], v[66:67], 0, s[44:45]
	s_xor_b64 s[44:45], s[20:21], s[6:7]
	s_xor_b64 s[46:47], s[28:29], s[20:21]
	s_xor_b64 s[48:49], s[28:29], s[0:1]
	s_xor_b64 s[50:51], s[28:29], s[2:3]
	s_xor_b64 s[52:53], s[28:29], s[4:5]
	s_xor_b64 s[54:55], s[28:29], s[6:7]
	v_readlane_b32 s77, v254, 2
	v_readlane_b32 s78, v254, 3
	v_readlane_b32 s79, v254, 4
	v_readlane_b32 s84, v254, 9
	v_readlane_b32 s85, v254, 10
	v_readlane_b32 s86, v254, 11
	v_readlane_b32 s87, v254, 12
	v_readlane_b32 s88, v254, 13
	v_readlane_b32 s89, v254, 14
	v_readlane_b32 s98, v254, 55
	s_lshl_b32 s98, s98, 6
	v_add_u32_e32 v228, s98, v130
	v_lshlrev_b32_e32 v228, 4, v228
	global_load_dwordx4 v[212:215], v228, s[36:37]
	global_load_dwordx4 v[224:227], v228, s[80:81]
	v_readlane_b32 s98, v255, 13
	v_readlane_b32 s99, v255, 14
	s_nop 4
	global_load_dwordx4 v[216:219], v228, s[98:99]
	v_readlane_b32 s98, v255, 15
	v_readlane_b32 s99, v255, 16
	s_nop 4
	global_load_dwordx4 v[220:223], v228, s[98:99]
	s_waitcnt vmcnt(3)
	ds_write_b128 v228, v[212:215]
	s_waitcnt vmcnt(2)
	ds_write_b128 v228, v[224:227] offset:24576
	s_waitcnt vmcnt(1)
	ds_write_b128 v228, v[216:219] offset:8192
	s_waitcnt vmcnt(0)
	ds_write_b128 v228, v[220:223] offset:16384
	s_waitcnt lgkmcnt(0)
	s_barrier
	s_branch .LBB0_1416

.LBB0_1425:
	s_add_i32 s56, s63, 0xffffff21
	s_waitcnt vmcnt(5)
	v_perm_b32 v106, v14, v6, s67
	v_perm_b32 v6, v14, v6, s68
	s_waitcnt vmcnt(3)
	v_perm_b32 v14, v46, v30, s67
	v_readlane_b32 s56, v105, s56
	v_perm_b32 v30, v46, v30, s68
	v_perm_b32 v46, v14, v106, s69
	v_perm_b32 v14, v14, v106, s33
	v_perm_b32 v106, v30, v6, s69
	v_perm_b32 v6, v30, v6, s33
	v_dot4c_i32_i8_e32 v74, s56, v14
	v_and_b32_e32 v14, 0xf0f0f0f0, v14
	v_dot4c_i32_i8_e32 v70, s56, v14
	v_and_b32_e32 v14, 0xf0f0f0f0, v106
	v_dot4c_i32_i8_e32 v76, s56, v6
	v_and_b32_e32 v6, 0xf0f0f0f0, v6
	v_and_b32_e32 v30, 0xf0f0f0f0, v46
	v_dot4c_i32_i8_e32 v72, s56, v14
	v_dot4c_i32_i8_e32 v73, s56, v6
	v_perm_b32 v6, v15, v7, s67
	v_perm_b32 v14, v47, v31, s67
	v_dot4c_i32_i8_e32 v69, s56, v30
	v_perm_b32 v7, v15, v7, s68
	v_perm_b32 v15, v47, v31, s68
	v_perm_b32 v30, v14, v6, s69
	v_perm_b32 v6, v14, v6, s33
	v_perm_b32 v14, v15, v7, s69
	v_dot4c_i32_i8_e32 v85, s56, v6
	v_and_b32_e32 v6, 0xf0f0f0f0, v6
	v_perm_b32 v7, v15, v7, s33
	v_dot4c_i32_i8_e32 v81, s56, v6
	v_and_b32_e32 v6, 0xf0f0f0f0, v14
	v_dot4c_i32_i8_e32 v82, s56, v6
	v_and_b32_e32 v6, 0xf0f0f0f0, v7
	v_and_b32_e32 v15, 0xf0f0f0f0, v30
	v_dot4c_i32_i8_e32 v94, s56, v7
	v_dot4c_i32_i8_e32 v84, s56, v6
	v_perm_b32 v6, v16, v8, s67
	v_perm_b32 v7, v16, v8, s68
	v_perm_b32 v8, v48, v32, s67
	v_dot4c_i32_i8_e32 v77, s56, v15
	v_dot4c_i32_i8_e32 v86, s56, v14
	v_perm_b32 v14, v48, v32, s68
	v_perm_b32 v15, v8, v6, s69
	v_perm_b32 v6, v8, v6, s33
	v_perm_b32 v8, v14, v7, s69
	v_dot4c_i32_i8_e32 v96, s56, v6
	v_and_b32_e32 v6, 0xf0f0f0f0, v6
	v_perm_b32 v7, v14, v7, s33
	v_dot4c_i32_i8_e32 v88, s56, v6
	v_and_b32_e32 v6, 0xf0f0f0f0, v8
	v_dot4c_i32_i8_e32 v89, s56, v6
	v_and_b32_e32 v6, 0xf0f0f0f0, v7
	v_and_b32_e32 v14, 0xf0f0f0f0, v15
	v_dot4c_i32_i8_e32 v97, s56, v8
	v_dot4c_i32_i8_e32 v90, s56, v6
	v_perm_b32 v6, v17, v9, s67
	v_perm_b32 v8, v49, v33, s67
	v_dot4c_i32_i8_e32 v87, s56, v14
	v_dot4c_i32_i8_e32 v98, s56, v7
	v_perm_b32 v7, v17, v9, s68
	v_perm_b32 v9, v49, v33, s68
	v_perm_b32 v14, v8, v6, s69
	v_perm_b32 v6, v8, v6, s33
	v_perm_b32 v8, v9, v7, s69
	v_dot4c_i32_i8_e32 v100, s56, v6
	v_and_b32_e32 v6, 0xf0f0f0f0, v6
	s_add_i32 s91, s63, -15
	v_perm_b32 v7, v9, v7, s33
	v_dot4c_i32_i8_e32 v92, s56, v6
	v_and_b32_e32 v6, 0xf0f0f0f0, v8
	s_cmp_gt_u32 s62, 2
	v_and_b32_e32 v9, 0xf0f0f0f0, v14
	v_dot4c_i32_i8_e32 v93, s56, v6
	v_and_b32_e32 v6, 0xf0f0f0f0, v7
	s_cselect_b64 vcc, -1, 0
	s_bitcmp0_b32 s91, 6
	v_dot4c_i32_i8_e32 v66, s56, v46
	v_dot4c_i32_i8_e32 v75, s56, v106
	v_dot4c_i32_i8_e32 v80, s56, v30
	v_dot4c_i32_i8_e32 v95, s56, v15
	v_dot4c_i32_i8_e32 v99, s56, v14
	v_dot4c_i32_i8_e32 v91, s56, v9
	v_dot4c_i32_i8_e32 v101, s56, v8
	v_dot4c_i32_i8_e32 v102, s56, v7
	v_dot4c_i32_i8_e32 v83, s56, v6
	s_cselect_b64 s[56:57], -1, 0
	v_cndmask_b32_e64 v6, v79, v78, s[56:57]
	v_cndmask_b32_e32 v6, v6, v199, vcc
	s_add_i32 s57, s90, 0xffe20000
	v_readlane_b32 s56, v6, s91
	s_lshl_b32 s56, s56, 10
	s_and_b32 s57, s57, 0x1000000
	s_add_i32 s56, s56, s57
	s_add_i32 s91, s63, -14
	s_bitcmp0_b32 s91, 6
	buffer_load_dwordx4 v[6:9], v0, s[92:95], s56 offen
	s_cselect_b64 s[56:57], -1, 0
	v_cndmask_b32_e64 v14, v79, v78, s[56:57]
	v_cndmask_b32_e32 v14, v14, v199, vcc
	s_add_i32 s57, s90, 0xffe40000
	v_readlane_b32 s56, v14, s91
	s_lshl_b32 s56, s56, 10
	s_and_b32 s57, s57, 0x1000000
	s_add_i32 s56, s56, s57
	s_add_i32 s91, s63, -13
	s_bitcmp0_b32 s91, 6
	buffer_load_dwordx4 v[14:17], v0, s[92:95], s56 offen
	s_cselect_b64 s[56:57], -1, 0
	v_cndmask_b32_e64 v30, v79, v78, s[56:57]
	v_cndmask_b32_e32 v30, v30, v199, vcc
	s_add_i32 s57, s90, 0xffe60000
	v_readlane_b32 s56, v30, s91
	s_lshl_b32 s56, s56, 10
	s_and_b32 s57, s57, 0x1000000
	s_add_i32 s56, s56, s57
	s_add_i32 s91, s63, -12
	s_bitcmp0_b32 s91, 6
	buffer_load_dwordx4 v[30:33], v0, s[92:95], s56 offen
	s_cselect_b64 s[56:57], -1, 0
	v_cndmask_b32_e64 v46, v79, v78, s[56:57]
	v_cndmask_b32_e32 v46, v46, v199, vcc
	s_add_i32 s57, s90, 0xffe80000
	v_readlane_b32 s56, v46, s91
	s_lshl_b32 s56, s56, 10
	s_and_b32 s57, s57, 0x1000000
	s_add_i32 s56, s56, s57
	s_nop 1
	buffer_load_dwordx4 v[46:49], v0, s[92:95], s56 offen
	s_add_i32 s56, s63, 0xffffff25
	s_waitcnt vmcnt(5)
	v_perm_b32 v106, v22, v2, s67
	v_perm_b32 v2, v22, v2, s68
	s_waitcnt vmcnt(3)
	v_perm_b32 v22, v54, v38, s67
	v_readlane_b32 s56, v105, s56
	v_perm_b32 v38, v54, v38, s68
	v_perm_b32 v54, v22, v106, s69
	v_perm_b32 v22, v22, v106, s33
	v_perm_b32 v106, v38, v2, s69
	v_perm_b32 v2, v38, v2, s33
	v_dot4c_i32_i8_e32 v74, s56, v22
	v_and_b32_e32 v22, 0xf0f0f0f0, v22
	v_dot4c_i32_i8_e32 v70, s56, v22
	v_and_b32_e32 v22, 0xf0f0f0f0, v106
	v_dot4c_i32_i8_e32 v76, s56, v2
	v_and_b32_e32 v2, 0xf0f0f0f0, v2
	v_and_b32_e32 v38, 0xf0f0f0f0, v54
	v_dot4c_i32_i8_e32 v72, s56, v22
	v_dot4c_i32_i8_e32 v73, s56, v2
	v_perm_b32 v2, v23, v3, s67
	v_perm_b32 v22, v55, v39, s67
	v_dot4c_i32_i8_e32 v69, s56, v38
	v_perm_b32 v3, v23, v3, s68
	v_perm_b32 v23, v55, v39, s68
	v_perm_b32 v38, v22, v2, s69
	v_perm_b32 v2, v22, v2, s33
	v_perm_b32 v22, v23, v3, s69
	v_dot4c_i32_i8_e32 v85, s56, v2
	v_and_b32_e32 v2, 0xf0f0f0f0, v2
	v_perm_b32 v3, v23, v3, s33
	v_dot4c_i32_i8_e32 v81, s56, v2
	v_and_b32_e32 v2, 0xf0f0f0f0, v22
	v_dot4c_i32_i8_e32 v82, s56, v2
	v_and_b32_e32 v2, 0xf0f0f0f0, v3
	v_and_b32_e32 v23, 0xf0f0f0f0, v38
	v_dot4c_i32_i8_e32 v94, s56, v3
	v_dot4c_i32_i8_e32 v84, s56, v2
	v_perm_b32 v2, v24, v4, s67
	v_perm_b32 v3, v24, v4, s68
	v_perm_b32 v4, v56, v40, s67
	v_dot4c_i32_i8_e32 v77, s56, v23
	v_dot4c_i32_i8_e32 v86, s56, v22
	v_perm_b32 v22, v56, v40, s68
	v_perm_b32 v23, v4, v2, s69
	v_perm_b32 v2, v4, v2, s33
	v_perm_b32 v4, v22, v3, s69
	v_dot4c_i32_i8_e32 v96, s56, v2
	v_and_b32_e32 v2, 0xf0f0f0f0, v2
	v_perm_b32 v3, v22, v3, s33
	v_dot4c_i32_i8_e32 v88, s56, v2
	v_and_b32_e32 v2, 0xf0f0f0f0, v4
	v_dot4c_i32_i8_e32 v89, s56, v2
	v_and_b32_e32 v2, 0xf0f0f0f0, v3
	v_and_b32_e32 v22, 0xf0f0f0f0, v23
	v_dot4c_i32_i8_e32 v97, s56, v4
	v_dot4c_i32_i8_e32 v90, s56, v2
	v_perm_b32 v2, v25, v5, s67
	v_perm_b32 v4, v57, v41, s67
	v_dot4c_i32_i8_e32 v87, s56, v22
	v_dot4c_i32_i8_e32 v98, s56, v3
	v_perm_b32 v3, v25, v5, s68
	v_perm_b32 v5, v57, v41, s68
	v_perm_b32 v22, v4, v2, s69
	v_perm_b32 v2, v4, v2, s33
	v_perm_b32 v4, v5, v3, s69
	v_dot4c_i32_i8_e32 v100, s56, v2
	v_and_b32_e32 v2, 0xf0f0f0f0, v2
	v_perm_b32 v3, v5, v3, s33
	v_dot4c_i32_i8_e32 v92, s56, v2
	v_and_b32_e32 v2, 0xf0f0f0f0, v4
	s_add_i32 s91, s63, -11
	v_and_b32_e32 v5, 0xf0f0f0f0, v22
	v_dot4c_i32_i8_e32 v93, s56, v2
	v_and_b32_e32 v2, 0xf0f0f0f0, v3
	s_bitcmp0_b32 s91, 6
	v_dot4c_i32_i8_e32 v66, s56, v54
	v_dot4c_i32_i8_e32 v75, s56, v106
	v_dot4c_i32_i8_e32 v80, s56, v38
	v_dot4c_i32_i8_e32 v95, s56, v23
	v_dot4c_i32_i8_e32 v99, s56, v22
	v_dot4c_i32_i8_e32 v91, s56, v5
	v_dot4c_i32_i8_e32 v101, s56, v4
	v_dot4c_i32_i8_e32 v102, s56, v3
	v_dot4c_i32_i8_e32 v83, s56, v2
	s_cselect_b64 s[56:57], -1, 0
	v_cndmask_b32_e64 v2, v79, v78, s[56:57]
	v_cndmask_b32_e32 v2, v2, v199, vcc
	s_add_i32 s57, s90, 0xffea0000
	v_readlane_b32 s56, v2, s91
	s_lshl_b32 s56, s56, 10
	s_and_b32 s57, s57, 0x1000000
	s_add_i32 s56, s56, s57
	s_add_i32 s91, s63, -10
	s_bitcmp0_b32 s91, 6
	buffer_load_dwordx4 v[2:5], v0, s[92:95], s56 offen
	s_cselect_b64 s[56:57], -1, 0
	v_cndmask_b32_e64 v22, v79, v78, s[56:57]
	v_cndmask_b32_e32 v22, v22, v199, vcc
	s_add_i32 s57, s90, 0xffec0000
	v_readlane_b32 s56, v22, s91
	s_lshl_b32 s56, s56, 10
	s_and_b32 s57, s57, 0x1000000
	s_add_i32 s56, s56, s57
	s_add_i32 s91, s63, -9
	s_bitcmp0_b32 s91, 6
	buffer_load_dwordx4 v[22:25], v0, s[92:95], s56 offen
	s_cselect_b64 s[56:57], -1, 0
	v_cndmask_b32_e64 v38, v79, v78, s[56:57]
	v_cndmask_b32_e32 v38, v38, v199, vcc
	s_add_i32 s57, s90, 0xffee0000
	v_readlane_b32 s56, v38, s91
	s_lshl_b32 s56, s56, 10
	s_and_b32 s57, s57, 0x1000000
	s_add_i32 s56, s56, s57
	s_add_i32 s91, s63, -8
	s_bitcmp0_b32 s91, 6
	buffer_load_dwordx4 v[38:41], v0, s[92:95], s56 offen
	s_cselect_b64 s[56:57], -1, 0
	v_cndmask_b32_e64 v54, v79, v78, s[56:57]
	v_cndmask_b32_e32 v54, v54, v199, vcc
	s_add_i32 s57, s90, 0xfff00000
	v_readlane_b32 s56, v54, s91
	s_lshl_b32 s56, s56, 10
	s_and_b32 s57, s57, 0x1000000
	s_add_i32 s56, s56, s57
	s_nop 1
	buffer_load_dwordx4 v[54:57], v0, s[92:95], s56 offen
	s_add_i32 s56, s63, 0xffffff29
	s_waitcnt vmcnt(5)
	v_perm_b32 v106, v26, v10, s67
	v_perm_b32 v10, v26, v10, s68
	s_waitcnt vmcnt(3)
	v_perm_b32 v26, v58, v42, s67
	v_readlane_b32 s56, v105, s56
	v_perm_b32 v42, v58, v42, s68
	v_perm_b32 v58, v26, v106, s69
	v_perm_b32 v26, v26, v106, s33
	v_perm_b32 v106, v42, v10, s69
	v_perm_b32 v10, v42, v10, s33
	v_dot4c_i32_i8_e32 v74, s56, v26
	v_and_b32_e32 v26, 0xf0f0f0f0, v26
	v_dot4c_i32_i8_e32 v70, s56, v26
	v_and_b32_e32 v26, 0xf0f0f0f0, v106
	v_dot4c_i32_i8_e32 v76, s56, v10
	v_and_b32_e32 v10, 0xf0f0f0f0, v10
	v_and_b32_e32 v42, 0xf0f0f0f0, v58
	v_dot4c_i32_i8_e32 v72, s56, v26
	v_dot4c_i32_i8_e32 v73, s56, v10
	v_perm_b32 v10, v27, v11, s67
	v_perm_b32 v26, v59, v43, s67
	v_dot4c_i32_i8_e32 v69, s56, v42
	v_perm_b32 v11, v27, v11, s68
	v_perm_b32 v27, v59, v43, s68
	v_perm_b32 v42, v26, v10, s69
	v_perm_b32 v10, v26, v10, s33
	v_perm_b32 v26, v27, v11, s69
	v_dot4c_i32_i8_e32 v85, s56, v10
	v_and_b32_e32 v10, 0xf0f0f0f0, v10
	v_perm_b32 v11, v27, v11, s33
	v_dot4c_i32_i8_e32 v81, s56, v10
	v_and_b32_e32 v10, 0xf0f0f0f0, v26
	v_dot4c_i32_i8_e32 v82, s56, v10
	v_and_b32_e32 v10, 0xf0f0f0f0, v11
	v_and_b32_e32 v27, 0xf0f0f0f0, v42
	v_dot4c_i32_i8_e32 v94, s56, v11
	v_dot4c_i32_i8_e32 v84, s56, v10
	v_perm_b32 v10, v28, v12, s67
	v_perm_b32 v11, v28, v12, s68
	v_perm_b32 v12, v60, v44, s67
	v_dot4c_i32_i8_e32 v77, s56, v27
	v_dot4c_i32_i8_e32 v86, s56, v26
	v_perm_b32 v26, v60, v44, s68
	v_perm_b32 v27, v12, v10, s69
	v_perm_b32 v10, v12, v10, s33
	v_perm_b32 v12, v26, v11, s69
	v_dot4c_i32_i8_e32 v96, s56, v10
	v_and_b32_e32 v10, 0xf0f0f0f0, v10
	v_perm_b32 v11, v26, v11, s33
	v_dot4c_i32_i8_e32 v88, s56, v10
	v_and_b32_e32 v10, 0xf0f0f0f0, v12
	v_dot4c_i32_i8_e32 v89, s56, v10
	v_and_b32_e32 v10, 0xf0f0f0f0, v11
	v_and_b32_e32 v26, 0xf0f0f0f0, v27
	v_dot4c_i32_i8_e32 v97, s56, v12
	v_dot4c_i32_i8_e32 v90, s56, v10
	v_perm_b32 v10, v29, v13, s67
	v_perm_b32 v12, v61, v45, s67
	v_dot4c_i32_i8_e32 v87, s56, v26
	v_dot4c_i32_i8_e32 v98, s56, v11
	v_perm_b32 v11, v29, v13, s68
	v_perm_b32 v13, v61, v45, s68
	v_perm_b32 v26, v12, v10, s69
	v_perm_b32 v10, v12, v10, s33
	v_perm_b32 v12, v13, v11, s69
	v_dot4c_i32_i8_e32 v100, s56, v10
	v_and_b32_e32 v10, 0xf0f0f0f0, v10
	v_perm_b32 v11, v13, v11, s33
	v_dot4c_i32_i8_e32 v92, s56, v10
	v_and_b32_e32 v10, 0xf0f0f0f0, v12
	s_add_i32 s91, s63, -7
	v_and_b32_e32 v13, 0xf0f0f0f0, v26
	v_dot4c_i32_i8_e32 v93, s56, v10
	v_and_b32_e32 v10, 0xf0f0f0f0, v11
	s_bitcmp0_b32 s91, 6
	v_dot4c_i32_i8_e32 v66, s56, v58
	v_dot4c_i32_i8_e32 v75, s56, v106
	v_dot4c_i32_i8_e32 v80, s56, v42
	v_dot4c_i32_i8_e32 v95, s56, v27
	v_dot4c_i32_i8_e32 v99, s56, v26
	v_dot4c_i32_i8_e32 v91, s56, v13
	v_dot4c_i32_i8_e32 v101, s56, v12
	v_dot4c_i32_i8_e32 v102, s56, v11
	v_dot4c_i32_i8_e32 v83, s56, v10
	s_cselect_b64 s[56:57], -1, 0
	v_cndmask_b32_e64 v10, v79, v78, s[56:57]
	v_cndmask_b32_e32 v10, v10, v199, vcc
	s_add_i32 s57, s90, 0xfff20000
	v_readlane_b32 s56, v10, s91
	s_lshl_b32 s56, s56, 10
	s_and_b32 s57, s57, 0x1000000
	s_add_i32 s56, s56, s57
	s_add_i32 s91, s63, -6
	s_bitcmp0_b32 s91, 6
	buffer_load_dwordx4 v[10:13], v0, s[92:95], s56 offen
	s_cselect_b64 s[56:57], -1, 0
	v_cndmask_b32_e64 v26, v79, v78, s[56:57]
	v_cndmask_b32_e32 v26, v26, v199, vcc
	s_add_i32 s57, s90, 0xfff40000
	v_readlane_b32 s56, v26, s91
	s_lshl_b32 s56, s56, 10
	s_and_b32 s57, s57, 0x1000000
	s_add_i32 s56, s56, s57
	s_add_i32 s91, s63, -5
	s_bitcmp0_b32 s91, 6
	buffer_load_dwordx4 v[26:29], v0, s[92:95], s56 offen
	s_cselect_b64 s[56:57], -1, 0
	v_cndmask_b32_e64 v42, v79, v78, s[56:57]
	v_cndmask_b32_e32 v42, v42, v199, vcc
	s_add_i32 s57, s90, 0xfff60000
	v_readlane_b32 s56, v42, s91
	s_lshl_b32 s56, s56, 10
	s_and_b32 s57, s57, 0x1000000
	s_add_i32 s56, s56, s57
	s_add_i32 s91, s63, -4
	s_bitcmp0_b32 s91, 6
	buffer_load_dwordx4 v[42:45], v0, s[92:95], s56 offen
	s_cselect_b64 s[56:57], -1, 0
	v_cndmask_b32_e64 v58, v79, v78, s[56:57]
	v_cndmask_b32_e32 v58, v58, v199, vcc
	s_add_i32 s57, s90, 0xfff80000
	v_readlane_b32 s56, v58, s91
	s_lshl_b32 s56, s56, 10
	s_and_b32 s57, s57, 0x1000000
	s_add_i32 s56, s56, s57
	s_nop 1
	buffer_load_dwordx4 v[58:61], v0, s[92:95], s56 offen
	s_add_i32 s56, s63, 0xffffff2d
	s_waitcnt vmcnt(5)
	v_perm_b32 v106, v34, v18, s67
	v_perm_b32 v18, v34, v18, s68
	s_waitcnt vmcnt(3)
	v_perm_b32 v34, v62, v50, s67
	v_readlane_b32 s56, v105, s56
	v_perm_b32 v50, v62, v50, s68
	v_perm_b32 v62, v34, v106, s69
	v_perm_b32 v34, v34, v106, s33
	v_perm_b32 v106, v50, v18, s69
	v_perm_b32 v18, v50, v18, s33
	v_dot4c_i32_i8_e32 v74, s56, v34
	v_and_b32_e32 v34, 0xf0f0f0f0, v34
	v_dot4c_i32_i8_e32 v70, s56, v34
	v_and_b32_e32 v34, 0xf0f0f0f0, v106
	v_dot4c_i32_i8_e32 v76, s56, v18
	v_and_b32_e32 v18, 0xf0f0f0f0, v18
	v_and_b32_e32 v50, 0xf0f0f0f0, v62
	v_dot4c_i32_i8_e32 v72, s56, v34
	v_dot4c_i32_i8_e32 v73, s56, v18
	v_perm_b32 v18, v35, v19, s67
	v_perm_b32 v34, v63, v51, s67
	v_dot4c_i32_i8_e32 v69, s56, v50
	v_perm_b32 v19, v35, v19, s68
	v_perm_b32 v35, v63, v51, s68
	v_perm_b32 v50, v34, v18, s69
	v_perm_b32 v18, v34, v18, s33
	v_perm_b32 v34, v35, v19, s69
	v_dot4c_i32_i8_e32 v85, s56, v18
	v_and_b32_e32 v18, 0xf0f0f0f0, v18
	v_perm_b32 v19, v35, v19, s33
	v_dot4c_i32_i8_e32 v81, s56, v18
	v_and_b32_e32 v18, 0xf0f0f0f0, v34
	v_dot4c_i32_i8_e32 v82, s56, v18
	v_and_b32_e32 v18, 0xf0f0f0f0, v19
	v_and_b32_e32 v35, 0xf0f0f0f0, v50
	v_dot4c_i32_i8_e32 v94, s56, v19
	v_dot4c_i32_i8_e32 v84, s56, v18
	v_perm_b32 v18, v36, v20, s67
	v_perm_b32 v19, v36, v20, s68
	v_perm_b32 v20, v64, v52, s67
	v_dot4c_i32_i8_e32 v77, s56, v35
	v_dot4c_i32_i8_e32 v86, s56, v34
	v_perm_b32 v34, v64, v52, s68
	v_perm_b32 v35, v20, v18, s69
	v_perm_b32 v18, v20, v18, s33
	v_perm_b32 v20, v34, v19, s69
	v_dot4c_i32_i8_e32 v96, s56, v18
	v_and_b32_e32 v18, 0xf0f0f0f0, v18
	v_perm_b32 v19, v34, v19, s33
	v_dot4c_i32_i8_e32 v88, s56, v18
	v_and_b32_e32 v18, 0xf0f0f0f0, v20
	v_dot4c_i32_i8_e32 v89, s56, v18
	v_and_b32_e32 v18, 0xf0f0f0f0, v19
	v_and_b32_e32 v34, 0xf0f0f0f0, v35
	v_dot4c_i32_i8_e32 v97, s56, v20
	v_dot4c_i32_i8_e32 v90, s56, v18
	v_perm_b32 v18, v37, v21, s67
	v_perm_b32 v20, v65, v53, s67
	v_dot4c_i32_i8_e32 v87, s56, v34
	v_dot4c_i32_i8_e32 v98, s56, v19
	v_perm_b32 v19, v37, v21, s68
	v_perm_b32 v21, v65, v53, s68
	v_perm_b32 v34, v20, v18, s69
	v_perm_b32 v18, v20, v18, s33
	v_perm_b32 v20, v21, v19, s69
	v_dot4c_i32_i8_e32 v100, s56, v18
	v_and_b32_e32 v18, 0xf0f0f0f0, v18
	v_perm_b32 v19, v21, v19, s33
	v_dot4c_i32_i8_e32 v92, s56, v18
	v_and_b32_e32 v18, 0xf0f0f0f0, v20
	s_add_i32 s91, s63, -3
	v_and_b32_e32 v21, 0xf0f0f0f0, v34
	v_dot4c_i32_i8_e32 v93, s56, v18
	v_and_b32_e32 v18, 0xf0f0f0f0, v19
	s_bitcmp0_b32 s91, 6
	v_dot4c_i32_i8_e32 v66, s56, v62
	v_dot4c_i32_i8_e32 v75, s56, v106
	v_dot4c_i32_i8_e32 v80, s56, v50
	v_dot4c_i32_i8_e32 v95, s56, v35
	v_dot4c_i32_i8_e32 v99, s56, v34
	v_dot4c_i32_i8_e32 v91, s56, v21
	v_dot4c_i32_i8_e32 v101, s56, v20
	v_dot4c_i32_i8_e32 v102, s56, v19
	v_dot4c_i32_i8_e32 v83, s56, v18
	s_cselect_b64 s[56:57], -1, 0
	v_cndmask_b32_e64 v18, v79, v78, s[56:57]
	v_cndmask_b32_e32 v18, v18, v199, vcc
	s_add_i32 s57, s90, 0xfffa0000
	v_readlane_b32 s56, v18, s91
	s_lshl_b32 s56, s56, 10
	s_and_b32 s57, s57, 0x1000000
	s_add_i32 s56, s56, s57
	s_add_i32 s91, s63, -2
	s_bitcmp0_b32 s91, 6
	buffer_load_dwordx4 v[18:21], v0, s[92:95], s56 offen
	s_cselect_b64 s[56:57], -1, 0
	v_cndmask_b32_e64 v34, v79, v78, s[56:57]
	v_cndmask_b32_e32 v34, v34, v199, vcc
	s_add_i32 s57, s90, 0xfffc0000
	v_readlane_b32 s56, v34, s91
	s_lshl_b32 s56, s56, 10
	s_and_b32 s57, s57, 0x1000000
	s_add_i32 s56, s56, s57
	s_add_i32 s91, s63, -1
	s_bitcmp0_b32 s91, 6
	buffer_load_dwordx4 v[34:37], v0, s[92:95], s56 offen
	s_cselect_b64 s[56:57], -1, 0
	v_cndmask_b32_e64 v50, v79, v78, s[56:57]
	v_cndmask_b32_e32 v50, v50, v199, vcc
	s_add_i32 s57, s90, 0xfffe0000
	v_readlane_b32 s56, v50, s91
	s_lshl_b32 s56, s56, 10
	s_and_b32 s57, s57, 0x1000000
	s_add_i32 s56, s56, s57
	s_bitcmp0_b32 s63, 6
	s_nop 0
	buffer_load_dwordx4 v[50:53], v0, s[92:95], s56 offen
	s_cselect_b64 s[56:57], -1, 0
	v_cndmask_b32_e64 v62, v79, v78, s[56:57]
	v_cndmask_b32_e32 v62, v62, v199, vcc
	s_and_b32 s57, s90, 0x1000000
	v_readlane_b32 s56, v62, s63
	s_lshl_b32 s56, s56, 10
	s_add_i32 s56, s56, s57
	s_nop 2
	buffer_load_dwordx4 v[62:65], v0, s[92:95], s56 offen
	s_add_i32 s62, s62, 1
	s_add_i32 s63, s63, 16
	s_add_i32 s90, s90, 0x200000
	s_cmpk_eq_i32 s63, 0x11f
	s_cbranch_scc0 .LBB0_1425
; __device__ __forceinline__ int ov(int x) { asm volatile("" : "+v"(x)); return x; }
;     ...
;         f32x2 acc[16];
;         { const float fsc = wm * (1.0f / 127.0f);
; #pragma unroll
;           for (int i = 0; i < 16; ++i) acc[i] = (f32x2){(float)(acci[2 * i] - acci[2 * i + 1] - c8) * fsc, (float)acci[2 * i + 1] * (fsc * 0.0625f)}; }
;         const int lane2 = ov(lane);
;         float s = 0.f;
; #pragma unroll
;         for (int hh = 0; hh < 4; ++hh) { float pl[8]; unpack8(*(const v4u*)(PLE + (size_t)t * D + lane2 * 32 + hh * 8), pl);
;             float z8[8]; unpack8(*(const v4u*)(ZB + (size_t)t * D + lane2 * 32 + hh * 8), z8);
;             f32x4 xa = (f32x4){z8[0], z8[1], z8[2], z8[3]}, xb = (f32x4){z8[4], z8[5], z8[6], z8[7]};
;             xa = (xa - mean1) * rstd1 * *(const f32x4*)(gain1 + lane2 * 32 + hh * 8) + *(const f32x4*)(bias1 + lane2 * 32 + hh * 8);
;             xb = (xb - mean1) * rstd1 * *(const f32x4*)(gain1 + lane2 * 32 + hh * 8 + 4) + *(const f32x4*)(bias1 + lane2 * 32 + hh * 8 + 4);
;             acc[hh * 4 + 0] += (f32x2){ALPHA * xa[0] + pl[0], ALPHA * xa[1] + pl[1]}; acc[hh * 4 + 1] += (f32x2){ALPHA * xa[2] + pl[2], ALPHA * xa[3] + pl[3]};
;             acc[hh * 4 + 2] += (f32x2){ALPHA * xb[0] + pl[4], ALPHA * xb[1] + pl[5]}; acc[hh * 4 + 3] += (f32x2){ALPHA * xb[2] + pl[6], ALPHA * xb[3] + pl[7]};
; #pragma unroll
;             for (int i = 0; i < 4; ++i) s += acc[hh * 4 + i].x + acc[hh * 4 + i].y; }
	s_waitcnt lgkmcnt(0)
	v_add_f32_e32 v78, v103, v104
	v_cvt_i32_f32_e32 v78, v78
	v_mov_b32_e32 v201, v130
	s_lshl_b64 s[56:57], s[86:87], 1
	v_lshlrev_b32_e32 v78, 3, v78
	v_sub_u32_e32 v78, 0, v78
	v_sub_u32_e32 v79, v78, v69
	v_add_u32_e32 v66, v79, v66
	v_sub_u32_e32 v79, v78, v70
	v_add_u32_e32 v74, v79, v74
	v_sub_u32_e32 v79, v78, v72
	v_add_u32_e32 v75, v79, v75
	v_sub_u32_e32 v79, v78, v73
	v_add_u32_e32 v76, v79, v76
	v_sub_u32_e32 v79, v78, v77
	v_add_u32_e32 v79, v79, v80
	v_sub_u32_e32 v80, v78, v81
	v_add_u32_e32 v80, v80, v85
	v_sub_u32_e32 v85, v78, v82
	v_add_u32_e32 v85, v85, v86
	v_sub_u32_e32 v86, v78, v84
	v_add_u32_e32 v86, v86, v94
	v_sub_u32_e32 v94, v78, v87
	v_add_u32_e32 v94, v94, v95
	v_sub_u32_e32 v95, v78, v88
	v_readlane_b32 s62, v255, 7
	v_lshlrev_b32_e32 v134, 5, v201
	v_add_u32_e32 v95, v95, v96
	v_sub_u32_e32 v96, v78, v89
	s_add_u32 s62, s62, s56
	v_readlane_b32 s63, v255, 9
	v_ashrrev_i32_e32 v135, 31, v134
	v_add_u32_e32 v96, v96, v97
	v_sub_u32_e32 v97, v78, v90
	v_cvt_f32_i32_e32 v181, v70
	v_mul_f32_e32 v142, 0x3c010204, v71
	s_addc_u32 s63, s63, s57
	v_lshlrev_b64 v[70:71], 1, v[134:135]
	v_add_u32_e32 v97, v97, v98
	v_sub_u32_e32 v98, v78, v91
	v_cvt_f32_i32_e32 v178, v75
	v_cvt_f32_i32_e32 v180, v74
	v_lshl_add_u64 v[74:75], s[62:63], 0, v[70:71]
	v_readlane_b32 s62, v254, 56
	v_add_u32_e32 v98, v98, v99
	v_sub_u32_e32 v99, v78, v92
	s_add_u32 s62, s62, s56
	v_readlane_b32 s63, v255, 5
	v_add_u32_e32 v99, v99, v100
	v_sub_u32_e32 v100, v78, v93
	v_sub_u32_e32 v78, v78, v83
	s_addc_u32 s63, s63, s57
	v_add_u32_e32 v100, v100, v101
	v_add_u32_e32 v78, v78, v102
	v_cvt_f32_i32_e32 v138, v99
	v_cvt_f32_i32_e32 v140, v98
	v_lshl_add_u64 v[98:99], s[62:63], 0, v[70:71]
	v_cvt_f32_i32_e32 v136, v100
	v_cvt_f32_i32_e32 v137, v93
	v_cvt_f32_i32_e32 v139, v92
	v_cvt_f32_i32_e32 v141, v91
	v_cvt_f32_i32_e32 v146, v97
	v_cvt_f32_i32_e32 v147, v90
	v_cvt_f32_i32_e32 v148, v96
	v_cvt_f32_i32_e32 v149, v89
	v_cvt_f32_i32_e32 v150, v95
	v_cvt_f32_i32_e32 v151, v88
	v_cvt_f32_i32_e32 v152, v94
	v_cvt_f32_i32_e32 v153, v87
	v_cvt_f32_i32_e32 v160, v86
	v_cvt_f32_i32_e32 v161, v84
	v_cvt_f32_i32_e32 v170, v85
	v_cvt_f32_i32_e32 v171, v82
	v_cvt_f32_i32_e32 v172, v80
	v_cvt_f32_i32_e32 v173, v81
	v_cvt_f32_i32_e32 v174, v79
	v_cvt_f32_i32_e32 v175, v77
	v_cvt_f32_i32_e32 v176, v76
	v_cvt_f32_i32_e32 v177, v73
	v_cvt_f32_i32_e32 v179, v72
	v_cvt_f32_i32_e32 v144, v78
	v_cvt_f32_i32_e32 v145, v83
	global_load_dwordx4 v[70:73], v[74:75], off offset:48
	global_load_dwordx4 v[78:81], v[74:75], off offset:32
	global_load_dwordx4 v[86:89], v[74:75], off offset:16
	global_load_dwordx4 v[90:93], v[74:75], off
	s_nop 0
	global_load_dwordx4 v[74:77], v[98:99], off offset:48
	global_load_dwordx4 v[82:85], v[98:99], off offset:32
	global_load_dwordx4 v[94:97], v[98:99], off offset:16
	s_nop 0
	global_load_dwordx4 v[98:101], v[98:99], off
	v_cvt_f32_i32_e32 v182, v66
	v_cvt_f32_i32_e32 v183, v69
	v_lshlrev_b64 v[154:155], 2, v[134:135]
	v_readlane_b32 s62, v255, 13
	v_lshl_add_u64 v[158:159], s[36:37], 0, v[154:155]
	v_readlane_b32 s63, v255, 14
	v_mul_f32_e32 v143, 0x3d800000, v142
	v_readlane_b32 s72, v254, 20
	v_lshl_add_u64 v[156:157], s[62:63], 0, v[154:155]
	v_readlane_b32 s73, v254, 21
	v_readlane_b32 s72, v255, 15
	v_readlane_b32 s73, v255, 16
	s_lshl_b64 s[62:63], s[86:87], 2
	v_readlane_b32 s74, v254, 22
	v_readlane_b32 s75, v254, 23
	s_add_u32 s62, s74, s62
	s_addc_u32 s63, s75, s63
	s_and_b64 vcc, exec, s[82:83]
	v_readlane_b32 s76, v254, 24
	v_readlane_b32 s77, v254, 25
	v_readlane_b32 s78, v254, 26
	v_readlane_b32 s79, v254, 27
	s_waitcnt vmcnt(0)
	v_lshlrev_b32_e32 v66, 16, v98
	v_and_b32_e32 v69, 0xffff0000, v98
	v_lshlrev_b32_e32 v98, 16, v99
	v_and_b32_e32 v99, 0xffff0000, v99
	v_lshlrev_b32_e32 v164, 16, v100
	v_and_b32_e32 v165, 0xffff0000, v100
	v_lshlrev_b32_e32 v166, 16, v101
	v_and_b32_e32 v167, 0xffff0000, v101
	v_sub_f32_e32 v99, v99, v67
	v_sub_f32_e32 v98, v98, v67
	v_sub_f32_e32 v101, v69, v67
	v_sub_f32_e32 v100, v66, v67
	v_pk_mul_f32 v[184:185], v[68:69], v[100:101] op_sel_hi:[0,1]
	v_pk_mul_f32 v[186:187], v[68:69], v[98:99] op_sel_hi:[0,1]
	ds_read_b128 v[98:101], v154 offset:48
	ds_read_b128 v[102:105], v154 offset:32
	ds_read_b128 v[106:109], v154 offset:16
	ds_read_b128 v[122:125], v154 offset:0
	ds_read_b128 v[110:113], v154 offset:8240
	ds_read_b128 v[114:117], v154 offset:8224
	ds_read_b128 v[118:121], v154 offset:8208
	ds_read_b128 v[126:129], v154 offset:8192
	s_waitcnt lgkmcnt(0)
;     ...
;         for (int hh = 0; hh < 4; ++hh) { float pl[8]; unpack8(*(const v4u*)(PLE + (size_t)t * D + lane2 * 32 + hh * 8), pl);
;             float z8[8]; unpack8(*(const v4u*)(ZB + (size_t)t * D + lane2 * 32 + hh * 8), z8);
;             f32x4 xa = (f32x4){z8[0], z8[1], z8[2], z8[3]}, xb = (f32x4){z8[4], z8[5], z8[6], z8[7]};
;             xa = (xa - mean1) * rstd1 * *(const f32x4*)(gain1 + lane2 * 32 + hh * 8) + *(const f32x4*)(bias1 + lane2 * 32 + hh * 8);
;             xb = (xb - mean1) * rstd1 * *(const f32x4*)(gain1 + lane2 * 32 + hh * 8 + 4) + *(const f32x4*)(bias1 + lane2 * 32 + hh * 8 + 4);
;             acc[hh * 4 + 0] += (f32x2){ALPHA * xa[0] + pl[0], ALPHA * xa[1] + pl[1]}; acc[hh * 4 + 1] += (f32x2){ALPHA * xa[2] + pl[2], ALPHA * xa[3] + pl[3]};
;             acc[hh * 4 + 2] += (f32x2){ALPHA * xb[0] + pl[4], ALPHA * xb[1] + pl[5]}; acc[hh * 4 + 3] += (f32x2){ALPHA * xb[2] + pl[6], ALPHA * xb[3] + pl[7]};
; #pragma unroll
;             for (int i = 0; i < 4; ++i) s += acc[hh * 4 + i].x + acc[hh * 4 + i].y; }
	v_pk_fma_f32 v[124:125], v[124:125], v[186:187], v[128:129]
	v_sub_f32_e32 v129, v165, v67
	v_sub_f32_e32 v128, v164, v67
	v_pk_mul_f32 v[128:129], v[68:69], v[128:129] op_sel_hi:[0,1]
	v_pk_fma_f32 v[122:123], v[122:123], v[184:185], v[126:127]
	v_sub_f32_e32 v127, v167, v67
	v_sub_f32_e32 v126, v166, v67
	v_pk_fma_f32 v[106:107], v[106:107], v[128:129], v[118:119]
	v_lshlrev_b32_e32 v118, 16, v90
	v_and_b32_e32 v119, 0xffff0000, v90
	v_lshlrev_b32_e32 v90, 16, v91
	v_and_b32_e32 v91, 0xffff0000, v91
	v_pk_mul_f32 v[126:127], v[68:69], v[126:127] op_sel_hi:[0,1]
	v_pk_fma_f32 v[90:91], v[124:125], s[58:59], v[90:91] op_sel_hi:[1,0,1]
	v_pk_fma_f32 v[108:109], v[108:109], v[126:127], v[120:121]
	v_pk_fma_f32 v[118:119], v[122:123], s[58:59], v[118:119] op_sel_hi:[1,0,1]
	v_pk_fma_f32 v[120:121], v[142:143], v[180:181], v[90:91]
	v_lshlrev_b32_e32 v90, 16, v92
	v_and_b32_e32 v91, 0xffff0000, v92
	v_pk_fma_f32 v[118:119], v[142:143], v[182:183], v[118:119]
	v_pk_fma_f32 v[90:91], v[106:107], s[58:59], v[90:91] op_sel_hi:[1,0,1]
	v_add_f32_e32 v66, v118, v119
	v_pk_fma_f32 v[122:123], v[142:143], v[178:179], v[90:91]
	v_lshlrev_b32_e32 v90, 16, v93
	v_and_b32_e32 v91, 0xffff0000, v93
	v_pk_fma_f32 v[90:91], v[108:109], s[58:59], v[90:91] op_sel_hi:[1,0,1]
	v_add_f32_e32 v66, 0, v66
	v_add_f32_e32 v69, v120, v121
	v_pk_fma_f32 v[124:125], v[142:143], v[176:177], v[90:91]
	v_add_f32_e32 v66, v69, v66
	v_add_f32_e32 v69, v122, v123
	v_add_f32_e32 v66, v69, v66
	v_add_f32_e32 v69, v124, v125
	v_lshlrev_b32_e32 v90, 16, v95
	v_and_b32_e32 v91, 0xffff0000, v95
	v_lshlrev_b32_e32 v106, 16, v96
	v_and_b32_e32 v96, 0xffff0000, v96
	v_add_f32_e32 v66, v69, v66
	v_lshlrev_b32_e32 v69, 16, v94
	v_and_b32_e32 v92, 0xffff0000, v94
	v_lshlrev_b32_e32 v94, 16, v97
	v_and_b32_e32 v95, 0xffff0000, v97
	v_sub_f32_e32 v91, v91, v67
	v_sub_f32_e32 v90, v90, v67
	v_sub_f32_e32 v97, v96, v67
	v_sub_f32_e32 v96, v106, v67
	v_sub_f32_e32 v93, v92, v67
	v_sub_f32_e32 v92, v69, v67
	v_pk_mul_f32 v[90:91], v[68:69], v[90:91] op_sel_hi:[0,1]
	v_pk_mul_f32 v[96:97], v[68:69], v[96:97] op_sel_hi:[0,1]
	v_pk_mul_f32 v[92:93], v[68:69], v[92:93] op_sel_hi:[0,1]
	v_pk_fma_f32 v[90:91], v[104:105], v[90:91], v[116:117]
	v_pk_fma_f32 v[96:97], v[98:99], v[96:97], v[110:111]
	v_lshlrev_b32_e32 v98, 16, v86
	v_and_b32_e32 v99, 0xffff0000, v86
	v_lshlrev_b32_e32 v86, 16, v87
	v_and_b32_e32 v87, 0xffff0000, v87
	v_pk_fma_f32 v[92:93], v[102:103], v[92:93], v[114:115]
	v_pk_fma_f32 v[86:87], v[90:91], s[58:59], v[86:87] op_sel_hi:[1,0,1]
	v_sub_f32_e32 v95, v95, v67
	v_sub_f32_e32 v94, v94, v67
	v_pk_fma_f32 v[92:93], v[92:93], s[58:59], v[98:99] op_sel_hi:[1,0,1]
	v_pk_fma_f32 v[116:117], v[142:143], v[172:173], v[86:87]
	v_lshlrev_b32_e32 v86, 16, v88
	v_and_b32_e32 v87, 0xffff0000, v88
	v_pk_mul_f32 v[94:95], v[68:69], v[94:95] op_sel_hi:[0,1]
	v_pk_fma_f32 v[114:115], v[142:143], v[174:175], v[92:93]
	v_pk_fma_f32 v[86:87], v[96:97], s[58:59], v[86:87] op_sel_hi:[1,0,1]
	v_pk_fma_f32 v[94:95], v[100:101], v[94:95], v[112:113]
	v_pk_fma_f32 v[126:127], v[142:143], v[170:171], v[86:87]
	v_lshlrev_b32_e32 v86, 16, v89
	v_and_b32_e32 v87, 0xffff0000, v89
	v_add_f32_e32 v69, v114, v115
	v_pk_fma_f32 v[86:87], v[94:95], s[58:59], v[86:87] op_sel_hi:[1,0,1]
	v_add_f32_e32 v66, v66, v69
	v_add_f32_e32 v69, v116, v117
	v_pk_fma_f32 v[128:129], v[142:143], v[160:161], v[86:87]
	v_add_f32_e32 v66, v69, v66
	v_add_f32_e32 v69, v126, v127
	v_add_f32_e32 v66, v69, v66
	v_add_f32_e32 v69, v128, v129
	v_lshlrev_b32_e32 v86, 16, v82
	v_and_b32_e32 v87, 0xffff0000, v82
	v_lshlrev_b32_e32 v82, 16, v83
	v_and_b32_e32 v83, 0xffff0000, v83
	v_add_f32_e32 v66, v69, v66
	v_lshlrev_b32_e32 v69, 16, v84
	v_and_b32_e32 v172, 0xffff0000, v84
	v_lshlrev_b32_e32 v173, 16, v85
	v_and_b32_e32 v174, 0xffff0000, v85
	v_sub_f32_e32 v83, v83, v67
	v_sub_f32_e32 v82, v82, v67
	v_sub_f32_e32 v85, v87, v67
	v_sub_f32_e32 v84, v86, v67
	v_pk_mul_f32 v[160:161], v[68:69], v[84:85] op_sel_hi:[0,1]
	v_pk_mul_f32 v[170:171], v[68:69], v[82:83] op_sel_hi:[0,1]
	ds_read_b128 v[82:85], v154 offset:112
	ds_read_b128 v[86:89], v154 offset:96
	ds_read_b128 v[90:93], v154 offset:80
	ds_read_b128 v[106:109], v154 offset:64
	ds_read_b128 v[94:97], v154 offset:8304
	ds_read_b128 v[98:101], v154 offset:8288
	ds_read_b128 v[102:105], v154 offset:8272
	ds_read_b128 v[110:113], v154 offset:8256
	s_waitcnt lgkmcnt(0)
;     ...
;         for (int hh = 0; hh < 4; ++hh) { float pl[8]; unpack8(*(const v4u*)(PLE + (size_t)t * D + lane2 * 32 + hh * 8), pl);
;             float z8[8]; unpack8(*(const v4u*)(ZB + (size_t)t * D + lane2 * 32 + hh * 8), z8);
;             f32x4 xa = (f32x4){z8[0], z8[1], z8[2], z8[3]}, xb = (f32x4){z8[4], z8[5], z8[6], z8[7]};
;             xa = (xa - mean1) * rstd1 * *(const f32x4*)(gain1 + lane2 * 32 + hh * 8) + *(const f32x4*)(bias1 + lane2 * 32 + hh * 8);
;             xb = (xb - mean1) * rstd1 * *(const f32x4*)(gain1 + lane2 * 32 + hh * 8 + 4) + *(const f32x4*)(bias1 + lane2 * 32 + hh * 8 + 4);
;             acc[hh * 4 + 0] += (f32x2){ALPHA * xa[0] + pl[0], ALPHA * xa[1] + pl[1]}; acc[hh * 4 + 1] += (f32x2){ALPHA * xa[2] + pl[2], ALPHA * xa[3] + pl[3]};
;             acc[hh * 4 + 2] += (f32x2){ALPHA * xb[0] + pl[4], ALPHA * xb[1] + pl[5]}; acc[hh * 4 + 3] += (f32x2){ALPHA * xb[2] + pl[6], ALPHA * xb[3] + pl[7]};
; #pragma unroll
;             for (int i = 0; i < 4; ++i) s += acc[hh * 4 + i].x + acc[hh * 4 + i].y; }
;         const float mean = wave_sum(s) * (1.0f / D); float q = 0.f;
	v_pk_fma_f32 v[108:109], v[108:109], v[170:171], v[112:113]
	v_sub_f32_e32 v113, v172, v67
	v_sub_f32_e32 v112, v69, v67
	v_pk_mul_f32 v[112:113], v[68:69], v[112:113] op_sel_hi:[0,1]
	v_pk_fma_f32 v[106:107], v[106:107], v[160:161], v[110:111]
	v_sub_f32_e32 v111, v174, v67
	v_sub_f32_e32 v110, v173, v67
	v_pk_fma_f32 v[90:91], v[90:91], v[112:113], v[102:103]
	v_lshlrev_b32_e32 v102, 16, v78
	v_and_b32_e32 v103, 0xffff0000, v78
	v_lshlrev_b32_e32 v78, 16, v79
	v_and_b32_e32 v79, 0xffff0000, v79
	v_pk_mul_f32 v[110:111], v[68:69], v[110:111] op_sel_hi:[0,1]
	v_pk_fma_f32 v[78:79], v[108:109], s[58:59], v[78:79] op_sel_hi:[1,0,1]
	v_pk_fma_f32 v[92:93], v[92:93], v[110:111], v[104:105]
	v_pk_fma_f32 v[102:103], v[106:107], s[58:59], v[102:103] op_sel_hi:[1,0,1]
	v_pk_fma_f32 v[104:105], v[142:143], v[150:151], v[78:79]
	v_lshlrev_b32_e32 v78, 16, v80
	v_and_b32_e32 v79, 0xffff0000, v80
	v_pk_fma_f32 v[102:103], v[142:143], v[152:153], v[102:103]
	v_pk_fma_f32 v[78:79], v[90:91], s[58:59], v[78:79] op_sel_hi:[1,0,1]
	v_add_f32_e32 v69, v102, v103
	v_pk_fma_f32 v[90:91], v[142:143], v[148:149], v[78:79]
	v_lshlrev_b32_e32 v78, 16, v81
	v_and_b32_e32 v79, 0xffff0000, v81
	v_pk_fma_f32 v[78:79], v[92:93], s[58:59], v[78:79] op_sel_hi:[1,0,1]
	v_add_f32_e32 v66, v66, v69
	v_add_f32_e32 v69, v104, v105
	v_pk_fma_f32 v[92:93], v[142:143], v[146:147], v[78:79]
	v_add_f32_e32 v66, v69, v66
	v_add_f32_e32 v69, v90, v91
	v_add_f32_e32 v66, v69, v66
	v_add_f32_e32 v69, v92, v93
	v_add_f32_e32 v106, v69, v66
	v_lshlrev_b32_e32 v66, 16, v74
	v_and_b32_e32 v69, 0xffff0000, v74
	v_lshlrev_b32_e32 v74, 16, v75
	v_and_b32_e32 v75, 0xffff0000, v75
	v_lshlrev_b32_e32 v80, 16, v76
	v_and_b32_e32 v81, 0xffff0000, v76
	v_lshlrev_b32_e32 v78, 16, v77
	v_and_b32_e32 v79, 0xffff0000, v77
	v_sub_f32_e32 v75, v75, v67
	v_sub_f32_e32 v74, v74, v67
	v_sub_f32_e32 v77, v69, v67
	v_sub_f32_e32 v76, v66, v67
	v_pk_mul_f32 v[74:75], v[68:69], v[74:75] op_sel_hi:[0,1]
	v_sub_f32_e32 v79, v79, v67
	v_sub_f32_e32 v78, v78, v67
	v_sub_f32_e32 v81, v81, v67
	v_sub_f32_e32 v80, v80, v67
	v_pk_mul_f32 v[76:77], v[68:69], v[76:77] op_sel_hi:[0,1]
	v_pk_fma_f32 v[74:75], v[88:89], v[74:75], v[100:101]
	v_pk_mul_f32 v[66:67], v[68:69], v[80:81] op_sel_hi:[0,1]
	v_pk_mul_f32 v[68:69], v[68:69], v[78:79] op_sel_hi:[0,1]
	v_lshlrev_b32_e32 v78, 16, v70
	v_and_b32_e32 v79, 0xffff0000, v70
	v_lshlrev_b32_e32 v70, 16, v71
	v_and_b32_e32 v71, 0xffff0000, v71
	v_pk_fma_f32 v[76:77], v[86:87], v[76:77], v[98:99]
	v_pk_fma_f32 v[70:71], v[74:75], s[58:59], v[70:71] op_sel_hi:[1,0,1]
	v_pk_fma_f32 v[68:69], v[84:85], v[68:69], v[96:97]
	v_pk_fma_f32 v[66:67], v[82:83], v[66:67], v[94:95]
	v_pk_fma_f32 v[76:77], v[76:77], s[58:59], v[78:79] op_sel_hi:[1,0,1]
	v_pk_fma_f32 v[96:97], v[142:143], v[138:139], v[70:71]
	v_lshlrev_b32_e32 v70, 16, v72
	v_and_b32_e32 v71, 0xffff0000, v72
	v_pk_fma_f32 v[94:95], v[142:143], v[140:141], v[76:77]
	v_pk_fma_f32 v[66:67], v[66:67], s[58:59], v[70:71] op_sel_hi:[1,0,1]
	v_lshlrev_b32_e32 v70, 16, v73
	v_and_b32_e32 v71, 0xffff0000, v73
	v_pk_fma_f32 v[68:69], v[68:69], s[58:59], v[70:71] op_sel_hi:[1,0,1]
	v_mov_b32_e32 v70, v96
	v_mov_b32_e32 v71, v94
	v_mov_b32_e32 v72, v97
	v_mov_b32_e32 v73, v95
	v_pk_add_f32 v[70:71], v[70:71], v[72:73]
	v_pk_fma_f32 v[66:67], v[142:143], v[136:137], v[66:67]
	v_pk_fma_f32 v[68:69], v[142:143], v[144:145], v[68:69]
	v_add_f32_e32 v71, v106, v71
	v_add_f32_e32 v74, v70, v71
	v_mov_b32_e32 v70, v68
	v_mov_b32_e32 v71, v66
	v_mov_b32_e32 v72, v69
	v_mov_b32_e32 v73, v67
	v_pk_add_f32 v[70:71], v[70:71], v[72:73]
	v_lshl_add_u64 v[100:101], s[72:73], 0, v[154:155]
	v_add_f32_e32 v71, v71, v74
	v_add_f32_e32 v70, v70, v71
	v_mov_b32_e32 v71, v1
	v_lshl_add_u64 v[98:99], s[62:63], 0, v[154:155]
	v_mbcnt_lo_u32_b32 v71, -1, v71
	v_mbcnt_hi_u32_b32 v71, -1, v71
	v_lshlrev_b32_e32 v71, 2, v71
	v_xor_b32_e32 v72, 0x80, v71
	ds_bpermute_b32 v72, v72, v70
	s_waitcnt lgkmcnt(0)
	v_add_f32_e32 v70, v70, v72
	v_xor_b32_e32 v72, 64, v71
	ds_bpermute_b32 v72, v72, v70
	s_waitcnt lgkmcnt(0)
	v_add_f32_e32 v70, v70, v72
	v_xor_b32_e32 v72, 32, v71
	ds_bpermute_b32 v72, v72, v70
	s_waitcnt lgkmcnt(0)
	v_add_f32_e32 v70, v70, v72
	v_xor_b32_e32 v72, 16, v71
	ds_bpermute_b32 v72, v72, v70
	s_waitcnt lgkmcnt(0)
	v_add_f32_e32 v70, v70, v72
	v_xor_b32_e32 v72, 8, v71
	ds_bpermute_b32 v72, v72, v70
	v_xor_b32_e32 v71, 4, v71
	s_waitcnt lgkmcnt(0)
	v_add_f32_e32 v70, v70, v72
	ds_bpermute_b32 v71, v71, v70
	s_waitcnt lgkmcnt(0)
; __device__ __forceinline__ float ln_rstd(float q) { return __builtin_amdgcn_rsqf((q + LN_EPS * (float)D) * (1.0f / D)); }
; __device__ __forceinline__ v4u pack8(const float (&v)[8]) { v4u o; o.x = pk2(v[0], v[1]); o.y = pk2(v[2], v[3]); o.z = pk2(v[4], v[5]); o.w = pk2(v[6], v[7]); return o; }
;     ...
;         const float mean = wave_sum(s) * (1.0f / D); float q = 0.f;
; #pragma unroll
;         for (int i = 0; i < 16; ++i) { acc[i].x -= mean; acc[i].y -= mean; q += acc[i].x * acc[i].x + acc[i].y * acc[i].y; }
;         const float rstd = ln_rstd(wave_sum(q));
; #pragma unroll
;         for (int hh = 0; hh < 4; ++hh) {
;             const int c = lane2 * 32 + hh * 8;
;             float y[8];
; #pragma unroll
;             for (int q4 = 0; q4 < 2; ++q4) { const f32x4 ga = *(const f32x4*)(gain + c + q4 * 4), ba = *(const f32x4*)(bias + c + q4 * 4);
;                 const f32x2 z0 = acc[hh * 4 + q4 * 2], z1 = acc[hh * 4 + q4 * 2 + 1];
;                 f32x4 yo; yo[0] = z0.x * rstd * ga[0] + ba[0]; yo[1] = z0.y * rstd * ga[1] + ba[1]; yo[2] = z1.x * rstd * ga[2] + ba[2]; yo[3] = z1.y * rstd * ga[3] + ba[3];
;                 if (OF) *(f32x4*)(OF + (size_t)t * D + c + q4 * 4) = yo;
;                 y[q4 * 4] = yo[0]; y[q4 * 4 + 1] = yo[1]; y[q4 * 4 + 2] = yo[2]; y[q4 * 4 + 3] = yo[3]; }
;             if (!OF) *(v4u*)(XB + (size_t)t * D + c) = pack8(y);
	v_add_f32_e32 v70, v70, v71
	v_mul_f32_e32 v110, 0x3a000000, v70
	v_pk_add_f32 v[86:87], v[90:91], v[110:111] op_sel_hi:[1,0] neg_lo:[0,1] neg_hi:[0,1]
	v_pk_add_f32 v[88:89], v[92:93], v[110:111] op_sel_hi:[1,0] neg_lo:[0,1] neg_hi:[0,1]
	v_pk_add_f32 v[90:91], v[94:95], v[110:111] op_sel_hi:[1,0] neg_lo:[0,1] neg_hi:[0,1]
	v_pk_add_f32 v[92:93], v[96:97], v[110:111] op_sel_hi:[1,0] neg_lo:[0,1] neg_hi:[0,1]
	v_pk_add_f32 v[96:97], v[66:67], v[110:111] op_sel_hi:[1,0] neg_lo:[0,1] neg_hi:[0,1]
	v_pk_add_f32 v[94:95], v[68:69], v[110:111] op_sel_hi:[1,0] neg_lo:[0,1] neg_hi:[0,1]
	v_mov_b32_e32 v69, v97
	v_mov_b32_e32 v68, v95
	v_mov_b32_e32 v66, v94
	v_mov_b32_e32 v67, v96
	v_pk_mul_f32 v[68:69], v[68:69], v[68:69]
	v_pk_add_f32 v[82:83], v[102:103], v[110:111] op_sel_hi:[1,0] neg_lo:[0,1] neg_hi:[0,1]
	v_pk_fma_f32 v[144:145], v[66:67], v[66:67], v[68:69]
	v_mov_b32_e32 v66, v1
	v_lshl_add_u64 v[102:103], s[80:81], 0, v[154:155]
	v_mbcnt_lo_u32_b32 v66, -1, v66
	v_mbcnt_hi_u32_b32 v66, -1, v66
	v_lshlrev_b32_e32 v66, 2, v66
	v_xor_b32_e32 v148, 0x80, v66
	v_xor_b32_e32 v149, 64, v66
	v_xor_b32_e32 v150, 32, v66
	v_xor_b32_e32 v151, 16, v66
	v_xor_b32_e32 v152, 8, v66
	v_xor_b32_e32 v153, 4, v66
	ds_read_b128 v[66:69], v154 offset:16384
	ds_read_b128 v[106:109], v154 offset:24576
	v_pk_add_f32 v[70:71], v[122:123], v[110:111] op_sel_hi:[1,0] neg_lo:[0,1] neg_hi:[0,1]
	v_pk_add_f32 v[72:73], v[124:125], v[110:111] op_sel_hi:[1,0] neg_lo:[0,1] neg_hi:[0,1]
	v_pk_add_f32 v[74:75], v[114:115], v[110:111] op_sel_hi:[1,0] neg_lo:[0,1] neg_hi:[0,1]
	v_pk_add_f32 v[76:77], v[116:117], v[110:111] op_sel_hi:[1,0] neg_lo:[0,1] neg_hi:[0,1]
	v_pk_add_f32 v[78:79], v[126:127], v[110:111] op_sel_hi:[1,0] neg_lo:[0,1] neg_hi:[0,1]
	v_pk_add_f32 v[80:81], v[128:129], v[110:111] op_sel_hi:[1,0] neg_lo:[0,1] neg_hi:[0,1]
	v_pk_add_f32 v[84:85], v[104:105], v[110:111] op_sel_hi:[1,0] neg_lo:[0,1] neg_hi:[0,1]
	v_pk_add_f32 v[118:119], v[118:119], v[110:111] op_sel_hi:[1,0] neg_lo:[0,1] neg_hi:[0,1]
	v_pk_add_f32 v[110:111], v[120:121], v[110:111] op_sel_hi:[1,0] neg_lo:[0,1] neg_hi:[0,1]
	v_pk_mul_f32 v[146:147], v[118:119], v[118:119]
	v_pk_mul_f32 v[120:121], v[110:111], v[110:111]
	v_pk_mul_f32 v[112:113], v[70:71], v[70:71]
	v_add_f32_e32 v120, v120, v121
	v_add_f32_e32 v121, v146, v147
	v_pk_mul_f32 v[122:123], v[72:73], v[72:73]
	v_add_f32_e32 v120, v121, v120
	v_add_f32_e32 v112, v112, v113
	v_pk_mul_f32 v[114:115], v[74:75], v[74:75]
	v_add_f32_e32 v112, v112, v120
	v_add_f32_e32 v113, v122, v123
	v_pk_mul_f32 v[116:117], v[76:77], v[76:77]
	v_add_f32_e32 v112, v113, v112
	v_add_f32_e32 v113, v114, v115
	v_pk_mul_f32 v[124:125], v[78:79], v[78:79]
	v_add_f32_e32 v112, v113, v112
	v_add_f32_e32 v113, v116, v117
	v_pk_mul_f32 v[126:127], v[80:81], v[80:81]
	v_add_f32_e32 v112, v113, v112
	v_add_f32_e32 v113, v124, v125
	v_pk_mul_f32 v[128:129], v[82:83], v[82:83]
	v_add_f32_e32 v112, v113, v112
	v_add_f32_e32 v113, v126, v127
	v_pk_mul_f32 v[104:105], v[84:85], v[84:85]
	v_add_f32_e32 v112, v113, v112
	v_add_f32_e32 v113, v128, v129
	v_pk_mul_f32 v[136:137], v[86:87], v[86:87]
	v_add_f32_e32 v112, v113, v112
	v_add_f32_e32 v104, v104, v105
	v_pk_mul_f32 v[138:139], v[88:89], v[88:89]
	v_add_f32_e32 v104, v104, v112
	v_add_f32_e32 v105, v136, v137
	v_pk_mul_f32 v[140:141], v[90:91], v[90:91]
	v_add_f32_e32 v104, v105, v104
	v_add_f32_e32 v105, v138, v139
	v_pk_mul_f32 v[142:143], v[92:93], v[92:93]
	v_add_f32_e32 v104, v105, v104
	v_add_f32_e32 v105, v140, v141
	v_add_f32_e32 v104, v105, v104
	v_add_f32_e32 v105, v142, v143
	v_add_f32_e32 v104, v105, v104
	v_add_f32_e32 v104, v145, v104
	v_add_f32_e32 v104, v144, v104
	ds_bpermute_b32 v105, v148, v104
	s_waitcnt lgkmcnt(0)
	v_add_f32_e32 v104, v104, v105
	ds_bpermute_b32 v105, v149, v104
	s_waitcnt lgkmcnt(0)
	v_add_f32_e32 v104, v104, v105
	ds_bpermute_b32 v105, v150, v104
	s_waitcnt lgkmcnt(0)
	v_add_f32_e32 v104, v104, v105
	ds_bpermute_b32 v105, v151, v104
	s_waitcnt lgkmcnt(0)
	v_add_f32_e32 v104, v104, v105
	ds_bpermute_b32 v105, v152, v104
	s_waitcnt lgkmcnt(0)
	v_add_f32_e32 v104, v104, v105
	ds_bpermute_b32 v105, v153, v104
	s_waitcnt lgkmcnt(0)
	v_add_f32_e32 v104, v104, v105
	v_add_f32_e32 v104, 0x3ca7c5ac, v104
	v_mul_f32_e32 v104, 0x3a000000, v104
	v_rsq_f32_e32 v104, v104
	s_nop 0
	v_pk_mul_f32 v[112:113], v[118:119], v[104:105] op_sel_hi:[1,0]
	s_waitcnt vmcnt(0)
	v_pk_fma_f32 v[66:67], v[66:67], v[112:113], v[106:107]
	v_pk_mul_f32 v[106:107], v[110:111], v[104:105] op_sel_hi:[1,0]
	s_nop 0
	v_pk_fma_f32 v[68:69], v[68:69], v[106:107], v[108:109]
	s_cbranch_vccz .LBB0_1428
	global_store_dwordx4 v[98:99], v[66:69], off
.LBB0_1428:
	ds_read_b128 v[106:109], v154 offset:16400
	ds_read_b128 v[110:113], v154 offset:24592
	v_mov_b32_e32 v105, v104
	v_readlane_b32 s62, v255, 11
	v_pk_mul_f32 v[70:71], v[70:71], v[104:105]
	s_add_u32 s90, s62, s56
	v_pk_mul_f32 v[72:73], v[72:73], v[104:105]
	s_addc_u32 s91, s43, s57
	s_mov_b64 s[62:63], -1
	s_andn2_b64 vcc, exec, s[82:83]
	s_waitcnt lgkmcnt(0)
	v_pk_fma_f32 v[70:71], v[70:71], v[106:107], v[110:111]
	v_cndmask_b32_e64 v106, 0, 1, s[82:83]
	v_pk_fma_f32 v[72:73], v[72:73], v[108:109], v[112:113]
	v_cmp_ne_u32_e64 s[56:57], 1, v106
	s_cbranch_vccnz .LBB0_1430
	s_mov_b64 s[62:63], 0
	global_store_dwordx4 v[98:99], v[70:73], off offset:16

; __device__ __forceinline__ v4u pack8(const float (&v)[8]) { v4u o; o.x = pk2(v[0], v[1]); o.y = pk2(v[2], v[3]); o.z = pk2(v[4], v[5]); o.w = pk2(v[6], v[7]); return o; }
;     ...
;         for (int hh = 0; hh < 4; ++hh) {
;             const int c = lane2 * 32 + hh * 8;
;             float y[8];
; #pragma unroll
;             for (int q4 = 0; q4 < 2; ++q4) { const f32x4 ga = *(const f32x4*)(gain + c + q4 * 4), ba = *(const f32x4*)(bias + c + q4 * 4);
;                 const f32x2 z0 = acc[hh * 4 + q4 * 2], z1 = acc[hh * 4 + q4 * 2 + 1];
;                 f32x4 yo; yo[0] = z0.x * rstd * ga[0] + ba[0]; yo[1] = z0.y * rstd * ga[1] + ba[1]; yo[2] = z1.x * rstd * ga[2] + ba[2]; yo[3] = z1.y * rstd * ga[3] + ba[3];
;                 if (OF) *(f32x4*)(OF + (size_t)t * D + c + q4 * 4) = yo;
;                 y[q4 * 4] = yo[0]; y[q4 * 4 + 1] = yo[1]; y[q4 * 4 + 2] = yo[2]; y[q4 * 4 + 3] = yo[3]; }
;             if (!OF) *(v4u*)(XB + (size_t)t * D + c) = pack8(y);
.LBB0_1432:
	ds_read_b128 v[108:111], v154 offset:16416
	s_nop 0
	ds_read_b128 v[112:115], v154 offset:24608
	v_pk_mul_f32 v[74:75], v[74:75], v[104:105]
	v_pk_mul_f32 v[76:77], v[76:77], v[104:105]
	s_and_b64 vcc, exec, s[56:57]
	s_waitcnt lgkmcnt(0)
	v_pk_fma_f32 v[74:75], v[74:75], v[108:109], v[112:113]
	v_pk_fma_f32 v[76:77], v[76:77], v[110:111], v[114:115]
	s_cbranch_vccnz .LBB0_1434
	global_store_dwordx4 v[98:99], v[74:77], off offset:32
.LBB0_1434:
	ds_read_b128 v[108:111], v154 offset:16432
	ds_read_b128 v[112:115], v154 offset:24624
	v_pk_mul_f32 v[78:79], v[78:79], v[104:105]
	v_pk_mul_f32 v[80:81], v[80:81], v[104:105]
	s_and_b64 vcc, exec, s[56:57]
	s_mov_b64 s[62:63], -1
	s_waitcnt lgkmcnt(0)
	v_pk_fma_f32 v[78:79], v[78:79], v[108:109], v[112:113]
	v_pk_fma_f32 v[80:81], v[80:81], v[110:111], v[114:115]
	s_cbranch_vccnz .LBB0_1436
	s_mov_b64 s[62:63], 0
	global_store_dwordx4 v[98:99], v[78:81], off offset:48

; __device__ __forceinline__ v4u pack8(const float (&v)[8]) { v4u o; o.x = pk2(v[0], v[1]); o.y = pk2(v[2], v[3]); o.z = pk2(v[4], v[5]); o.w = pk2(v[6], v[7]); return o; }
;     ...
;         for (int hh = 0; hh < 4; ++hh) {
;             const int c = lane2 * 32 + hh * 8;
;             float y[8];
; #pragma unroll
;             for (int q4 = 0; q4 < 2; ++q4) { const f32x4 ga = *(const f32x4*)(gain + c + q4 * 4), ba = *(const f32x4*)(bias + c + q4 * 4);
;                 const f32x2 z0 = acc[hh * 4 + q4 * 2], z1 = acc[hh * 4 + q4 * 2 + 1];
;                 f32x4 yo; yo[0] = z0.x * rstd * ga[0] + ba[0]; yo[1] = z0.y * rstd * ga[1] + ba[1]; yo[2] = z1.x * rstd * ga[2] + ba[2]; yo[3] = z1.y * rstd * ga[3] + ba[3];
;                 if (OF) *(f32x4*)(OF + (size_t)t * D + c + q4 * 4) = yo;
;                 y[q4 * 4] = yo[0]; y[q4 * 4 + 1] = yo[1]; y[q4 * 4 + 2] = yo[2]; y[q4 * 4 + 3] = yo[3]; }
;             if (!OF) *(v4u*)(XB + (size_t)t * D + c) = pack8(y);
.LBB0_1438:
	ds_read_b128 v[108:111], v154 offset:16448
	s_nop 0
	ds_read_b128 v[112:115], v154 offset:24640
	v_pk_mul_f32 v[82:83], v[82:83], v[104:105]
	v_pk_mul_f32 v[84:85], v[84:85], v[104:105]
	s_and_b64 vcc, exec, s[56:57]
	s_waitcnt lgkmcnt(0)
	v_pk_fma_f32 v[82:83], v[82:83], v[108:109], v[112:113]
	v_pk_fma_f32 v[84:85], v[84:85], v[110:111], v[114:115]
	s_cbranch_vccnz .LBB0_1440
	global_store_dwordx4 v[98:99], v[82:85], off offset:64
.LBB0_1440:
	ds_read_b128 v[108:111], v154 offset:16464
	ds_read_b128 v[112:115], v154 offset:24656
	v_pk_mul_f32 v[86:87], v[86:87], v[104:105]
	v_pk_mul_f32 v[88:89], v[88:89], v[104:105]
	s_and_b64 vcc, exec, s[56:57]
	s_mov_b64 s[62:63], -1
	s_waitcnt lgkmcnt(0)
	v_pk_fma_f32 v[86:87], v[86:87], v[108:109], v[112:113]
	v_pk_fma_f32 v[88:89], v[88:89], v[110:111], v[114:115]
	s_cbranch_vccnz .LBB0_1442
	s_mov_b64 s[62:63], 0
	global_store_dwordx4 v[98:99], v[86:89], off offset:80

; __device__ __forceinline__ v4u pack8(const float (&v)[8]) { v4u o; o.x = pk2(v[0], v[1]); o.y = pk2(v[2], v[3]); o.z = pk2(v[4], v[5]); o.w = pk2(v[6], v[7]); return o; }
;     ...
;         for (int hh = 0; hh < 4; ++hh) {
;             const int c = lane2 * 32 + hh * 8;
;             float y[8];
; #pragma unroll
;             for (int q4 = 0; q4 < 2; ++q4) { const f32x4 ga = *(const f32x4*)(gain + c + q4 * 4), ba = *(const f32x4*)(bias + c + q4 * 4);
;                 const f32x2 z0 = acc[hh * 4 + q4 * 2], z1 = acc[hh * 4 + q4 * 2 + 1];
;                 f32x4 yo; yo[0] = z0.x * rstd * ga[0] + ba[0]; yo[1] = z0.y * rstd * ga[1] + ba[1]; yo[2] = z1.x * rstd * ga[2] + ba[2]; yo[3] = z1.y * rstd * ga[3] + ba[3];
;                 if (OF) *(f32x4*)(OF + (size_t)t * D + c + q4 * 4) = yo;
;                 y[q4 * 4] = yo[0]; y[q4 * 4 + 1] = yo[1]; y[q4 * 4 + 2] = yo[2]; y[q4 * 4 + 3] = yo[3]; }
;             if (!OF) *(v4u*)(XB + (size_t)t * D + c) = pack8(y);
.LBB0_1444:
	ds_read_b128 v[108:111], v154 offset:16480
	s_nop 0
	ds_read_b128 v[112:115], v154 offset:24672
	v_pk_mul_f32 v[90:91], v[90:91], v[104:105]
	v_pk_mul_f32 v[92:93], v[92:93], v[104:105]
	s_and_b64 vcc, exec, s[56:57]
	s_waitcnt lgkmcnt(0)
	v_pk_fma_f32 v[90:91], v[90:91], v[108:109], v[112:113]
	v_pk_fma_f32 v[92:93], v[92:93], v[110:111], v[114:115]
	s_cbranch_vccnz .LBB0_1446
	global_store_dwordx4 v[98:99], v[90:93], off offset:96
.LBB0_1446:
	ds_read_b128 v[108:111], v154 offset:16496
	s_nop 0
	ds_read_b128 v[100:103], v154 offset:24688
	v_pk_mul_f32 v[96:97], v[96:97], v[104:105]
	v_pk_mul_f32 v[104:105], v[94:95], v[104:105]
	s_and_b64 vcc, exec, s[56:57]
	s_mov_b64 s[56:57], -1
	s_waitcnt lgkmcnt(0)
	v_pk_fma_f32 v[94:95], v[96:97], v[108:109], v[100:101]
	v_pk_fma_f32 v[96:97], v[104:105], v[110:111], v[102:103]
	s_cbranch_vccnz .LBB0_1448
	s_mov_b64 s[56:57], 0
	global_store_dwordx4 v[98:99], v[94:97], off offset:112
